# P1 PROJ epilogue stores with sc1 (write-through)
# baseline (speedup 1.0000x reference)
.LBB0_139:
	v_and_b32_e32 v138, 0xc0, v227
	v_lshl_or_b32 v138, s52, 8, v138
	v_mov_b32_e32 v201, v200
	s_waitcnt lgkmcnt(2)
	v_lshl_or_b32 v186, v228, 3, v138
	v_mov_b32_e32 v138, v200
	v_mov_b32_e32 v139, v200
	v_pk_mul_f32 v[144:145], v[184:185], v[138:139]
	v_pk_mul_f32 v[142:143], v[182:183], v[200:201]
	v_pk_mul_f32 v[178:179], v[178:179], v[200:201]
	v_pk_mul_f32 v[180:181], v[180:181], v[138:139]
	v_cvt_pk_bf16_f32 v138, v190, v191
	v_cvt_pk_bf16_f32 v139, v192, v193
	v_cvt_pk_bf16_f32 v140, v202, v203
	v_cvt_pk_bf16_f32 v141, v188, v189
	v_cvt_pk_bf16_f32 v142, v142, v143
	v_cvt_pk_bf16_f32 v143, v144, v145
	v_cvt_pk_bf16_f32 v144, v178, v179
	s_nop 0
	v_cvt_pk_bf16_f32 v145, v180, v181
	ds_read_b32 v178, v226 offset:64
	v_ashrrev_i32_e32 v199, 31, v198
	v_lshlrev_b64 v[204:205], 12, v[198:199]
	s_waitcnt lgkmcnt(1)
	v_ashrrev_i32_e32 v187, 31, v186
	v_lshl_add_u64 v[180:181], s[18:19], 0, v[204:205]
	v_lshl_add_u64 v[180:181], v[186:187], 1, v[180:181]
	s_waitcnt lgkmcnt(0)
	v_pk_mul_f32 v[176:177], v[176:177], v[178:179] op_sel_hi:[1,0]
	v_pk_mul_f32 v[174:175], v[174:175], v[178:179] op_sel_hi:[1,0]
	v_pk_mul_f32 v[172:173], v[172:173], v[178:179] op_sel_hi:[1,0]
	s_and_b64 vcc, exec, s[10:11]
	v_pk_mul_f32 v[170:171], v[170:171], v[178:179] op_sel_hi:[1,0]
	global_store_dwordx4 v[180:181], v[138:141], off sc1
	global_store_dwordx4 v[180:181], v[142:145], off offset:64 sc1
	s_cbranch_vccnz .LBB0_143
	v_and_b32_e32 v139, 64, v225
	v_xor_b32_e32 v138, 16, v225
	v_add_u32_e32 v139, 64, v139
	v_cmp_lt_i32_e32 vcc, v138, v139
	s_nop 1
	v_cndmask_b32_e32 v138, v225, v138, vcc
	v_lshlrev_b32_e32 v138, 2, v138
	ds_bpermute_b32 v188, v138, v174
	ds_bpermute_b32 v182, v138, v170
	ds_bpermute_b32 v189, v138, v175
	ds_bpermute_b32 v183, v138, v171
	ds_bpermute_b32 v184, v138, v176
	ds_bpermute_b32 v180, v138, v172
	ds_bpermute_b32 v185, v138, v177
	ds_bpermute_b32 v181, v138, v173
	s_and_saveexec_b64 s[52:53], s[6:7]
	s_cbranch_execz .LBB0_142
	v_cndmask_b32_e64 v140, 1.0, -1.0, s[8:9]
	v_pk_mul_f32 v[138:139], v[96:97], v[140:141] op_sel_hi:[1,0]
	v_pk_mul_f32 v[140:141], v[94:95], v[140:141] op_sel_hi:[1,0]
	s_waitcnt lgkmcnt(5)
	v_pk_mul_f32 v[140:141], v[140:141], v[188:189]
	s_waitcnt lgkmcnt(1)
	v_pk_mul_f32 v[138:139], v[138:139], v[184:185]
	v_pk_fma_f32 v[174:175], v[230:231], v[174:175], v[140:141]
	v_pk_fma_f32 v[176:177], v[232:233], v[176:177], v[138:139]
	v_cndmask_b32_e64 v140, 1.0, -1.0, s[8:9]
	v_pk_mul_f32 v[138:139], v[88:89], v[140:141] op_sel_hi:[1,0]
	v_pk_mul_f32 v[140:141], v[86:87], v[140:141] op_sel_hi:[1,0]
	v_pk_mul_f32 v[140:141], v[140:141], v[182:183]
	s_waitcnt lgkmcnt(0)
	v_pk_mul_f32 v[138:139], v[138:139], v[180:181]
	v_pk_fma_f32 v[170:171], v[194:195], v[170:171], v[140:141]
	v_pk_fma_f32 v[172:173], v[196:197], v[172:173], v[138:139]

.LBB0_143:
	v_or_b32_e32 v138, 16, v198
	v_ashrrev_i32_e32 v139, 31, v138
	v_mov_b32_e32 v179, v178
	s_waitcnt lgkmcnt(0)
	v_lshlrev_b64 v[180:181], 12, v[138:139]
	v_mov_b32_e32 v138, v178
	v_mov_b32_e32 v139, v178
	v_pk_mul_f32 v[144:145], v[168:169], v[138:139]
	v_pk_mul_f32 v[142:143], v[166:167], v[178:179]
	v_pk_mul_f32 v[162:163], v[162:163], v[178:179]
	v_pk_mul_f32 v[164:165], v[164:165], v[138:139]
	v_cvt_pk_bf16_f32 v138, v174, v175
	v_cvt_pk_bf16_f32 v139, v176, v177
	v_cvt_pk_bf16_f32 v140, v170, v171
	v_cvt_pk_bf16_f32 v141, v172, v173
	v_cvt_pk_bf16_f32 v142, v142, v143
	v_cvt_pk_bf16_f32 v143, v144, v145
	v_cvt_pk_bf16_f32 v144, v162, v163
	s_nop 0
	v_cvt_pk_bf16_f32 v145, v164, v165
	ds_read_b32 v162, v226 offset:128
	v_lshl_add_u64 v[164:165], s[18:19], 0, v[180:181]
	v_lshl_add_u64 v[164:165], v[186:187], 1, v[164:165]
	s_and_b64 vcc, exec, s[10:11]
	global_store_dwordx4 v[164:165], v[138:141], off sc1
	global_store_dwordx4 v[164:165], v[142:145], off offset:64 sc1
	s_waitcnt lgkmcnt(0)
	v_pk_mul_f32 v[160:161], v[160:161], v[162:163] op_sel_hi:[1,0]
	v_pk_mul_f32 v[158:159], v[158:159], v[162:163] op_sel_hi:[1,0]
	v_pk_mul_f32 v[156:157], v[156:157], v[162:163] op_sel_hi:[1,0]
	v_pk_mul_f32 v[154:155], v[154:155], v[162:163] op_sel_hi:[1,0]
	s_cbranch_vccnz .LBB0_147
	v_and_b32_e32 v139, 64, v225
	v_xor_b32_e32 v138, 16, v225
	v_add_u32_e32 v139, 64, v139
	v_cmp_lt_i32_e32 vcc, v138, v139
	s_nop 1
	v_cndmask_b32_e32 v138, v225, v138, vcc
	v_lshlrev_b32_e32 v138, 2, v138
	ds_bpermute_b32 v170, v138, v158
	ds_bpermute_b32 v166, v138, v154
	ds_bpermute_b32 v171, v138, v159
	ds_bpermute_b32 v167, v138, v155
	ds_bpermute_b32 v168, v138, v160
	ds_bpermute_b32 v164, v138, v156
	ds_bpermute_b32 v169, v138, v161
	ds_bpermute_b32 v165, v138, v157
	s_and_saveexec_b64 s[52:53], s[6:7]
	s_cbranch_execz .LBB0_146
	v_cndmask_b32_e64 v140, 1.0, -1.0, s[8:9]
	v_pk_mul_f32 v[138:139], v[72:73], v[140:141] op_sel_hi:[1,0]
	v_pk_mul_f32 v[140:141], v[70:71], v[140:141] op_sel_hi:[1,0]
	s_waitcnt lgkmcnt(5)
	v_pk_mul_f32 v[140:141], v[140:141], v[170:171]
	s_waitcnt lgkmcnt(1)
	v_pk_mul_f32 v[138:139], v[138:139], v[168:169]
	v_pk_fma_f32 v[158:159], v[62:63], v[158:159], v[140:141]
	v_pk_fma_f32 v[160:161], v[64:65], v[160:161], v[138:139]
	v_cndmask_b32_e64 v140, 1.0, -1.0, s[8:9]
	v_pk_mul_f32 v[138:139], v[68:69], v[140:141] op_sel_hi:[1,0]
	v_pk_mul_f32 v[140:141], v[66:67], v[140:141] op_sel_hi:[1,0]
	v_pk_mul_f32 v[140:141], v[140:141], v[166:167]
	s_waitcnt lgkmcnt(0)
	v_pk_mul_f32 v[138:139], v[138:139], v[164:165]
	v_pk_fma_f32 v[154:155], v[58:59], v[154:155], v[140:141]
	v_pk_fma_f32 v[156:157], v[60:61], v[156:157], v[138:139]

.LBB0_147:
	v_or_b32_e32 v138, 32, v198
	v_ashrrev_i32_e32 v139, 31, v138
	v_mov_b32_e32 v163, v162
	s_waitcnt lgkmcnt(0)
	v_lshlrev_b64 v[164:165], 12, v[138:139]
	v_mov_b32_e32 v138, v162
	v_mov_b32_e32 v139, v162
	v_pk_mul_f32 v[144:145], v[152:153], v[138:139]
	v_pk_mul_f32 v[142:143], v[150:151], v[162:163]
	v_pk_mul_f32 v[146:147], v[146:147], v[162:163]
	v_pk_mul_f32 v[148:149], v[148:149], v[138:139]
	v_cvt_pk_bf16_f32 v138, v158, v159
	v_cvt_pk_bf16_f32 v139, v160, v161
	v_cvt_pk_bf16_f32 v140, v154, v155
	v_cvt_pk_bf16_f32 v141, v156, v157
	v_cvt_pk_bf16_f32 v142, v142, v143
	v_cvt_pk_bf16_f32 v143, v144, v145
	v_cvt_pk_bf16_f32 v144, v146, v147
	s_nop 0
	v_cvt_pk_bf16_f32 v145, v148, v149
	ds_read_b32 v146, v226 offset:192
	v_lshl_add_u64 v[148:149], s[18:19], 0, v[164:165]
	v_lshl_add_u64 v[148:149], v[186:187], 1, v[148:149]
	global_store_dwordx4 v[148:149], v[138:141], off sc1
	global_store_dwordx4 v[148:149], v[142:145], off offset:64 sc1
	s_and_b64 vcc, exec, s[10:11]
	s_waitcnt lgkmcnt(0)
	v_pk_mul_f32 v[140:141], v[100:101], v[146:147] op_sel_hi:[1,0]
	v_pk_mul_f32 v[144:145], v[104:105], v[146:147] op_sel_hi:[1,0]
	v_pk_mul_f32 v[142:143], v[102:103], v[146:147] op_sel_hi:[1,0]
	v_pk_mul_f32 v[138:139], v[98:99], v[146:147] op_sel_hi:[1,0]
	s_cbranch_vccnz .LBB0_151
	v_and_b32_e32 v99, 64, v225
	v_xor_b32_e32 v98, 16, v225
	v_add_u32_e32 v99, 64, v99
	v_cmp_lt_i32_e32 vcc, v98, v99
	s_nop 1
	v_cndmask_b32_e32 v98, v225, v98, vcc
	v_lshlrev_b32_e32 v98, 2, v98
	ds_bpermute_b32 v154, v98, v142
	ds_bpermute_b32 v150, v98, v138
	ds_bpermute_b32 v155, v98, v143
	ds_bpermute_b32 v151, v98, v139
	ds_bpermute_b32 v152, v98, v144
	ds_bpermute_b32 v148, v98, v140
	ds_bpermute_b32 v153, v98, v145
	ds_bpermute_b32 v149, v98, v141
	s_and_saveexec_b64 s[52:53], s[6:7]
	s_cbranch_execz .LBB0_150
	v_cndmask_b32_e64 v100, 1.0, -1.0, s[8:9]
	v_pk_mul_f32 v[98:99], v[48:49], v[100:101] op_sel_hi:[1,0]
	v_pk_mul_f32 v[100:101], v[46:47], v[100:101] op_sel_hi:[1,0]
	s_waitcnt lgkmcnt(5)
	v_pk_mul_f32 v[100:101], v[100:101], v[154:155]
	s_waitcnt lgkmcnt(1)
	v_pk_mul_f32 v[98:99], v[98:99], v[152:153]
	v_pk_fma_f32 v[142:143], v[42:43], v[142:143], v[100:101]
	v_pk_fma_f32 v[144:145], v[44:45], v[144:145], v[98:99]
	v_cndmask_b32_e64 v100, 1.0, -1.0, s[8:9]
	v_pk_mul_f32 v[98:99], v[36:37], v[100:101] op_sel_hi:[1,0]
	v_pk_mul_f32 v[100:101], v[34:35], v[100:101] op_sel_hi:[1,0]
	v_pk_mul_f32 v[100:101], v[100:101], v[150:151]
	s_waitcnt lgkmcnt(0)
	v_pk_mul_f32 v[98:99], v[98:99], v[148:149]
	v_pk_fma_f32 v[138:139], v[26:27], v[138:139], v[100:101]
	v_pk_fma_f32 v[140:141], v[28:29], v[140:141], v[98:99]

.LBB0_151:
	v_or_b32_e32 v98, 48, v198
	v_ashrrev_i32_e32 v99, 31, v98
	v_lshlrev_b64 v[98:99], 12, v[98:99]
	v_lshl_add_u64 v[98:99], s[18:19], 0, v[98:99]
	v_mov_b32_e32 v147, v146
	s_waitcnt lgkmcnt(0)
	v_lshl_add_u64 v[148:149], v[186:187], 1, v[98:99]
	v_mov_b32_e32 v98, v146
	v_mov_b32_e32 v99, v146
	v_pk_mul_f32 v[104:105], v[136:137], v[98:99]
	v_pk_mul_f32 v[102:103], v[134:135], v[146:147]
	s_and_b64 vcc, exec, s[10:11]
	v_pk_mul_f32 v[132:133], v[132:133], v[98:99]
	v_pk_mul_f32 v[130:131], v[130:131], v[146:147]
	v_cvt_pk_bf16_f32 v98, v142, v143
	v_cvt_pk_bf16_f32 v99, v144, v145
	v_cvt_pk_bf16_f32 v100, v138, v139
	v_cvt_pk_bf16_f32 v101, v140, v141
	v_cvt_pk_bf16_f32 v102, v102, v103
	v_cvt_pk_bf16_f32 v103, v104, v105
	s_nop 0
	v_cvt_pk_bf16_f32 v104, v130, v131
	v_cvt_pk_bf16_f32 v105, v132, v133
	global_store_dwordx4 v[148:149], v[98:101], off sc1
	global_store_dwordx4 v[148:149], v[102:105], off offset:64 sc1
	s_cbranch_vccnz .LBB0_155
	s_and_saveexec_b64 s[52:53], s[6:7]
	s_cbranch_execz .LBB0_154
	v_lshlrev_b64 v[26:27], 6, v[198:199]
	v_lshl_add_u64 v[26:27], s[20:21], 0, v[26:27]
	v_add_co_u32_e32 v34, vcc, 0x2000, v26
	v_lshl_add_u64 v[28:29], v[26:27], 0, s[28:29]
	s_nop 0
	v_addc_co_u32_e32 v35, vcc, 0, v27, vcc
	ds_read_b128 v[122:125], v255 offset:8192
	ds_read_b128 v[118:121], v255 offset:8240
	ds_read_b128 v[126:129], v255 offset:8224
	ds_read_b128 v[114:117], v255 offset:8208
	v_lshl_add_u64 v[28:29], v[26:27], 0, s[30:31]
	v_lshl_add_u64 v[66:67], v[26:27], 0, s[34:35]
	v_lshl_add_u64 v[26:27], v[26:27], 0, s[36:37]
	ds_read_b128 v[86:89], v255 offset:9264
	ds_read_b128 v[94:97], v255 offset:9248
	ds_read_b128 v[230:233], v255 offset:9216
	ds_read_b128 v[62:65], v255 offset:10240
	ds_read_b128 v[70:73], v255 offset:10272
	ds_read_b128 v[58:61], v255 offset:10256
	ds_read_b128 v[194:197], v255 offset:9232
	ds_read_b128 v[42:45], v255 offset:11264
	s_nop 0
	ds_read_b128 v[34:37], v255 offset:11312
	ds_read_b128 v[46:49], v255 offset:11296
	s_nop 0
	ds_read_b128 v[66:69], v255 offset:10288
	s_nop 0
	ds_read_b128 v[26:29], v255 offset:11280
	s_waitcnt lgkmcnt(0)

.LBB0_159:
	v_lshlrev_b64 v[98:99], 12, v[198:199]
	v_lshl_add_u64 v[98:99], s[18:19], 0, v[98:99]
	v_mov_b32_e32 v131, v130
	s_waitcnt lgkmcnt(0)
	v_lshl_add_u64 v[106:107], v[186:187], 1, v[98:99]
	v_mov_b32_e32 v98, v130
	v_mov_b32_e32 v99, v130
	v_pk_mul_f32 v[100:101], v[92:93], v[98:99]
	v_pk_mul_f32 v[82:83], v[82:83], v[130:131]
	v_pk_mul_f32 v[104:105], v[90:91], v[130:131]
	v_pk_mul_f32 v[84:85], v[84:85], v[98:99]
	v_cvt_pk_bf16_f32 v90, v134, v135
	v_cvt_pk_bf16_f32 v91, v132, v133
	v_cvt_pk_bf16_f32 v92, v110, v111
	v_cvt_pk_bf16_f32 v93, v108, v109
	v_cvt_pk_bf16_f32 v98, v104, v105
	v_cvt_pk_bf16_f32 v99, v100, v101
	v_cvt_pk_bf16_f32 v100, v82, v83
	s_nop 0
	v_cvt_pk_bf16_f32 v101, v84, v85
	ds_read_b32 v82, v226 offset:576
	v_add_co_u32_e32 v84, vcc, s74, v106
	v_lshl_add_u64 v[102:103], v[106:107], 0, s[38:39]
	s_nop 0
	v_addc_co_u32_e32 v85, vcc, 0, v107, vcc
	s_waitcnt lgkmcnt(0)
	v_pk_mul_f32 v[80:81], v[80:81], v[82:83] op_sel_hi:[1,0]
	v_pk_mul_f32 v[78:79], v[78:79], v[82:83] op_sel_hi:[1,0]
	v_pk_mul_f32 v[76:77], v[76:77], v[82:83] op_sel_hi:[1,0]
	s_and_b64 vcc, exec, s[10:11]
	v_pk_mul_f32 v[74:75], v[74:75], v[82:83] op_sel_hi:[1,0]
	global_store_dwordx4 v[84:85], v[90:93], off sc1
	global_store_dwordx4 v[102:103], v[98:101], off offset:64 sc1
	s_cbranch_vccnz .LBB0_163
	v_and_b32_e32 v84, 64, v225
	v_xor_b32_e32 v83, 16, v225
	v_add_u32_e32 v84, 64, v84
	v_cmp_lt_i32_e32 vcc, v83, v84
	s_nop 1
	v_cndmask_b32_e32 v83, v225, v83, vcc
	v_lshlrev_b32_e32 v83, 2, v83
	ds_bpermute_b32 v108, v83, v78
	ds_bpermute_b32 v90, v83, v74
	ds_bpermute_b32 v109, v83, v79
	ds_bpermute_b32 v91, v83, v75
	ds_bpermute_b32 v92, v83, v80
	ds_bpermute_b32 v84, v83, v76
	ds_bpermute_b32 v93, v83, v81
	ds_bpermute_b32 v85, v83, v77
	s_and_saveexec_b64 s[52:53], s[6:7]
	s_cbranch_execz .LBB0_162
	v_xor_b32_e32 v83, 0x80000000, v94
	v_xor_b32_e32 v98, 0x80000000, v95
	v_xor_b32_e32 v99, 0x80000000, v96
	v_xor_b32_e32 v100, 0x80000000, v97
	v_cndmask_b32_e64 v97, v97, v100, s[8:9]
	v_cndmask_b32_e64 v96, v96, v99, s[8:9]
	v_cndmask_b32_e64 v95, v95, v98, s[8:9]
	v_cndmask_b32_e64 v94, v94, v83, s[8:9]
	s_waitcnt lgkmcnt(5)
	v_pk_mul_f32 v[94:95], v[94:95], v[108:109]
	s_waitcnt lgkmcnt(1)
	v_pk_mul_f32 v[92:93], v[96:97], v[92:93]
	v_pk_fma_f32 v[78:79], v[230:231], v[78:79], v[94:95]
	v_pk_fma_f32 v[80:81], v[232:233], v[80:81], v[92:93]
	v_xor_b32_e32 v83, 0x80000000, v86
	v_xor_b32_e32 v92, 0x80000000, v87
	v_xor_b32_e32 v93, 0x80000000, v88
	v_xor_b32_e32 v94, 0x80000000, v89
	v_cndmask_b32_e64 v89, v89, v94, s[8:9]
	v_cndmask_b32_e64 v88, v88, v93, s[8:9]
	v_cndmask_b32_e64 v87, v87, v92, s[8:9]
	v_cndmask_b32_e64 v86, v86, v83, s[8:9]
	v_pk_mul_f32 v[86:87], v[86:87], v[90:91]
	s_waitcnt lgkmcnt(0)
	v_pk_mul_f32 v[84:85], v[88:89], v[84:85]
	v_pk_fma_f32 v[74:75], v[194:195], v[74:75], v[86:87]
	v_pk_fma_f32 v[76:77], v[196:197], v[76:77], v[84:85]

.LBB0_163:
	v_mov_b32_e32 v83, v82
	v_mov_b32_e32 v86, v82
	v_mov_b32_e32 v87, v82
	v_pk_mul_f32 v[50:51], v[50:51], v[82:83]
	v_pk_mul_f32 v[56:57], v[56:57], v[86:87]
	v_pk_mul_f32 v[88:89], v[54:55], v[82:83]
	v_pk_mul_f32 v[86:87], v[52:53], v[86:87]
	v_cvt_pk_bf16_f32 v52, v78, v79
	v_cvt_pk_bf16_f32 v53, v80, v81
	v_cvt_pk_bf16_f32 v54, v74, v75
	v_cvt_pk_bf16_f32 v55, v76, v77
	v_cvt_pk_bf16_f32 v74, v88, v89
	v_cvt_pk_bf16_f32 v75, v56, v57
	v_cvt_pk_bf16_f32 v76, v50, v51
	s_nop 0
	v_cvt_pk_bf16_f32 v77, v86, v87
	ds_read_b32 v50, v226 offset:640
	v_add_co_u32_e32 v56, vcc, s75, v106
	s_waitcnt lgkmcnt(1)
	v_lshl_add_u64 v[84:85], v[106:107], 0, s[40:41]
	v_addc_co_u32_e32 v57, vcc, 0, v107, vcc
	global_store_dwordx4 v[56:57], v[52:55], off sc1
	global_store_dwordx4 v[84:85], v[74:77], off offset:64 sc1
	s_waitcnt lgkmcnt(0)
	v_pk_mul_f32 v[40:41], v[40:41], v[50:51] op_sel_hi:[1,0]
	v_pk_mul_f32 v[38:39], v[38:39], v[50:51] op_sel_hi:[1,0]
	v_pk_mul_f32 v[32:33], v[32:33], v[50:51] op_sel_hi:[1,0]
	s_and_b64 vcc, exec, s[10:11]
	v_pk_mul_f32 v[52:53], v[30:31], v[50:51] op_sel_hi:[1,0]
	s_cbranch_vccnz .LBB0_167
	v_and_b32_e32 v31, 64, v225
	v_xor_b32_e32 v30, 16, v225
	v_add_u32_e32 v31, 64, v31
	v_cmp_lt_i32_e32 vcc, v30, v31
	s_nop 1
	v_cndmask_b32_e32 v30, v225, v30, vcc
	v_lshlrev_b32_e32 v31, 2, v30
	ds_bpermute_b32 v74, v31, v38
	ds_bpermute_b32 v54, v31, v52
	ds_bpermute_b32 v75, v31, v39
	ds_bpermute_b32 v55, v31, v53
	ds_bpermute_b32 v56, v31, v40
	ds_bpermute_b32 v30, v31, v32
	ds_bpermute_b32 v57, v31, v41
	ds_bpermute_b32 v31, v31, v33
	s_and_saveexec_b64 s[52:53], s[6:7]
	s_cbranch_execz .LBB0_166
	v_xor_b32_e32 v51, 0x80000000, v70
	v_xor_b32_e32 v76, 0x80000000, v71
	v_xor_b32_e32 v77, 0x80000000, v72
	v_xor_b32_e32 v78, 0x80000000, v73
	v_cndmask_b32_e64 v73, v73, v78, s[8:9]
	v_cndmask_b32_e64 v72, v72, v77, s[8:9]
	v_cndmask_b32_e64 v71, v71, v76, s[8:9]
	v_cndmask_b32_e64 v70, v70, v51, s[8:9]
	s_waitcnt lgkmcnt(5)
	v_pk_mul_f32 v[70:71], v[70:71], v[74:75]
	s_waitcnt lgkmcnt(1)
	v_pk_mul_f32 v[56:57], v[72:73], v[56:57]
	v_pk_fma_f32 v[38:39], v[62:63], v[38:39], v[70:71]
	v_pk_fma_f32 v[40:41], v[64:65], v[40:41], v[56:57]
	v_xor_b32_e32 v51, 0x80000000, v66
	v_xor_b32_e32 v62, 0x80000000, v67
	v_xor_b32_e32 v56, 0x80000000, v68
	v_xor_b32_e32 v57, 0x80000000, v69
	v_cndmask_b32_e64 v57, v69, v57, s[8:9]
	v_cndmask_b32_e64 v56, v68, v56, s[8:9]
	v_cndmask_b32_e64 v63, v67, v62, s[8:9]
	v_cndmask_b32_e64 v62, v66, v51, s[8:9]
	v_pk_mul_f32 v[54:55], v[62:63], v[54:55]
	s_waitcnt lgkmcnt(0)
	v_pk_mul_f32 v[30:31], v[56:57], v[30:31]
	v_pk_fma_f32 v[52:53], v[58:59], v[52:53], v[54:55]
	v_pk_fma_f32 v[32:33], v[60:61], v[32:33], v[30:31]

.LBB0_167:
	v_mov_b32_e32 v51, v50
	s_waitcnt lgkmcnt(3)
	v_mov_b32_e32 v56, v50
	s_waitcnt lgkmcnt(1)
	v_mov_b32_e32 v57, v50
	v_pk_mul_f32 v[18:19], v[18:19], v[50:51]
	s_waitcnt lgkmcnt(0)
	v_lshlrev_b64 v[30:31], 12, v[198:199]
	v_pk_mul_f32 v[24:25], v[24:25], v[56:57]
	v_pk_mul_f32 v[58:59], v[22:23], v[50:51]
	v_pk_mul_f32 v[56:57], v[20:21], v[56:57]
	v_cvt_pk_bf16_f32 v20, v38, v39
	v_cvt_pk_bf16_f32 v21, v40, v41
	v_cvt_pk_bf16_f32 v22, v52, v53
	v_cvt_pk_bf16_f32 v23, v32, v33
	v_cvt_pk_bf16_f32 v38, v58, v59
	v_cvt_pk_bf16_f32 v39, v24, v25
	v_cvt_pk_bf16_f32 v40, v18, v19
	s_nop 0
	v_cvt_pk_bf16_f32 v41, v56, v57
	ds_read_b32 v18, v226 offset:704
	v_lshl_add_u64 v[30:31], s[18:19], 0, v[30:31]
	v_lshl_add_u64 v[30:31], v[186:187], 1, v[30:31]
	v_add_co_u32_e32 v24, vcc, s76, v30
	s_waitcnt lgkmcnt(0)
	v_pk_mul_f32 v[16:17], v[16:17], v[18:19] op_sel_hi:[1,0]
	v_addc_co_u32_e32 v25, vcc, 0, v31, vcc
	v_pk_mul_f32 v[14:15], v[14:15], v[18:19] op_sel_hi:[1,0]
	v_pk_mul_f32 v[12:13], v[12:13], v[18:19] op_sel_hi:[1,0]
	s_and_b64 vcc, exec, s[10:11]
	v_pk_mul_f32 v[10:11], v[10:11], v[18:19] op_sel_hi:[1,0]
	v_lshl_add_u64 v[54:55], v[30:31], 0, s[42:43]
	global_store_dwordx4 v[24:25], v[20:23], off sc1
	global_store_dwordx4 v[54:55], v[38:41], off offset:64 sc1
	s_cbranch_vccnz .LBB0_171
	v_and_b32_e32 v20, 64, v225
	v_xor_b32_e32 v19, 16, v225
	v_add_u32_e32 v20, 64, v20
	v_cmp_lt_i32_e32 vcc, v19, v20
	s_nop 1
	v_cndmask_b32_e32 v19, v225, v19, vcc
	v_lshlrev_b32_e32 v19, 2, v19
	ds_bpermute_b32 v32, v19, v14
	ds_bpermute_b32 v22, v19, v10
	ds_bpermute_b32 v33, v19, v15
	ds_bpermute_b32 v23, v19, v11
	ds_bpermute_b32 v24, v19, v16
	ds_bpermute_b32 v20, v19, v12
	ds_bpermute_b32 v25, v19, v17
	ds_bpermute_b32 v21, v19, v13
	s_and_saveexec_b64 s[10:11], s[6:7]
	s_cbranch_execz .LBB0_170
	v_xor_b32_e32 v19, 0x80000000, v46
	v_xor_b32_e32 v40, 0x80000000, v47
	v_xor_b32_e32 v38, 0x80000000, v48
	v_xor_b32_e32 v39, 0x80000000, v49
	v_cndmask_b32_e64 v39, v49, v39, s[8:9]
	v_cndmask_b32_e64 v38, v48, v38, s[8:9]
	v_cndmask_b32_e64 v41, v47, v40, s[8:9]
	v_cndmask_b32_e64 v40, v46, v19, s[8:9]
	s_waitcnt lgkmcnt(5)
	v_pk_mul_f32 v[32:33], v[40:41], v[32:33]
	s_waitcnt lgkmcnt(1)
	v_pk_mul_f32 v[24:25], v[38:39], v[24:25]
	v_pk_fma_f32 v[14:15], v[42:43], v[14:15], v[32:33]
	v_pk_fma_f32 v[16:17], v[44:45], v[16:17], v[24:25]
	v_xor_b32_e32 v19, 0x80000000, v34
	v_xor_b32_e32 v32, 0x80000000, v35
	v_xor_b32_e32 v24, 0x80000000, v36
	v_xor_b32_e32 v25, 0x80000000, v37
	v_cndmask_b32_e64 v25, v37, v25, s[8:9]
	v_cndmask_b32_e64 v24, v36, v24, s[8:9]
	v_cndmask_b32_e64 v33, v35, v32, s[8:9]
	v_cndmask_b32_e64 v32, v34, v19, s[8:9]
	v_pk_mul_f32 v[22:23], v[32:33], v[22:23]
	s_waitcnt lgkmcnt(0)
	v_pk_mul_f32 v[20:21], v[24:25], v[20:21]
	v_pk_fma_f32 v[10:11], v[26:27], v[10:11], v[22:23]
	v_pk_fma_f32 v[12:13], v[28:29], v[12:13], v[20:21]

.LBB0_171:
	v_mov_b32_e32 v19, v18
	s_waitcnt lgkmcnt(2)
	v_mov_b32_e32 v20, v18
	s_waitcnt lgkmcnt(0)
	v_mov_b32_e32 v21, v18
	v_pk_mul_f32 v[22:23], v[8:9], v[20:21]
	v_pk_mul_f32 v[8:9], v[6:7], v[18:19]
	v_pk_mul_f32 v[20:21], v[4:5], v[20:21]
	v_pk_mul_f32 v[6:7], v[2:3], v[18:19]
	v_cvt_pk_bf16_f32 v2, v14, v15
	v_cvt_pk_bf16_f32 v3, v16, v17
	v_cvt_pk_bf16_f32 v4, v10, v11
	v_add_co_u32_e32 v10, vcc, 0xb0000, v30
	v_cvt_pk_bf16_f32 v5, v12, v13
	v_lshl_add_u64 v[18:19], v[30:31], 0, s[44:45]
	s_nop 0
	v_addc_co_u32_e32 v11, vcc, 0, v31, vcc
	s_and_b64 vcc, exec, s[4:5]
	s_mov_b64 s[4:5], -1
	v_cvt_pk_bf16_f32 v6, v6, v7
	v_cvt_pk_bf16_f32 v7, v20, v21
	v_cvt_pk_bf16_f32 v8, v8, v9
	v_cvt_pk_bf16_f32 v9, v22, v23
	global_store_dwordx4 v[10:11], v[2:5], off sc1
	global_store_dwordx4 v[18:19], v[6:9], off offset:64 sc1
	s_cbranch_vccnz .LBB0_118
	s_andn2_b64 vcc, exec, s[12:13]
	s_cbranch_vccnz .LBB0_174
	s_ashr_i32 s49, s48, 31
	s_lshl_b64 s[4:5], s[48:49], 10
	s_add_u32 s4, s0, s4
	s_addc_u32 s5, s1, s5
	s_lshl_b32 s6, s77, 10
	s_and_b32 s6, s6, 0x400
	s_add_i32 s6, s6, 0
	s_add_i32 s6, s6, 0x24cc0
	s_mov_b32 m0, s6
	s_nop 0
	global_load_lds_dwordx4 v210, s[4:5] offset:0
